# v8 with unit 0 included in the per-XCD rotation (mod 11)
# speedup vs baseline: 1.0044x; 1.0044x over previous
.Lstg_done_proj:
	v_mov_b32_e32 v1, v0
	v_mov_b32_e32 v6, v0
	s_cmpk_lt_i32 s94, 0xb00
	s_cselect_b64 s[0:1], -1, 0
	s_cmpk_gt_i32 s94, 0xaff
	v_readfirstlane_b32 s3, v6
	s_cbranch_scc1 .LBB0_272
	s_mov_b32 s6, s94
	s_cmp_lg_u32 s97, 0x100
	s_cbranch_scc1 .Lrot0_skip
	s_and_b32 s6, s94, 7
	s_lshl_b32 s6, s6, 8
	s_add_i32 s6, s6, s94
.Lrot0_skip:
	s_ashr_i32 s2, s6, 31
	s_lshr_b32 s2, s2, 29
	s_add_i32 s2, s6, s2
	s_ashr_i32 s4, s2, 3
	s_and_b32 s2, s2, -8
	s_sub_i32 s2, s6, s2
	s_cmp_lt_i32 s2, 0
	s_movk_i32 s5, 0x161
	s_cselect_b32 s5, s5, 0x160
	s_mul_i32 s2, s5, s2
	s_add_i32 s2, s2, s4
	s_mul_hi_i32 s4, s2, 0x2e8ba2e9
	s_lshr_b32 s5, s4, 31
	s_ashr_i32 s4, s4, 6
	s_add_i32 s4, s4, s5
	s_lshl_b32 s5, s4, 3
	s_mulk_i32 s4, 0x160
	s_sub_i32 s2, s2, s4
	s_sext_i32_i16 s4, s2
	s_bfe_u32 s4, s4, 0x3001c
	s_add_i32 s4, s2, s4
	s_sext_i32_i16 s6, s4
	s_and_b32 s4, s4, 0xfff8
	s_sub_i32 s2, s2, s4
	s_sext_i32_i16 s2, s2
	s_add_i32 s2, s5, s2
	s_ashr_i32 s72, s6, 3

.LBB0_278:
	s_add_i32 s48, s48, 1
	v_readlane_b32 s9, v255, 8
	s_mul_i32 s3, s48, s91
	s_mul_hi_u32 s8, s48, s9
	s_add_i32 s3, s8, s3
	s_mul_i32 s8, s48, s9
	s_add_u32 s8, s8, s94
	s_addc_u32 s9, s3, s92
	v_cmp_gt_i64_e32 vcc, s[8:9], v[208:209]
	v_cmp_lt_i64_e64 s[10:11], s[8:9], v[206:207]
	s_cbranch_vccnz .LBB0_280
	v_readlane_b32 s3, v255, 8
	s_nop 0
	s_cmp_lg_u32 s3, 0x100
	s_cbranch_scc1 .Lrot_skip
	s_and_b32 s3, s94, 7
	s_add_i32 s3, s3, s48
	s_cmp_ge_u32 s3, 11
	s_cbranch_scc0 .Lrot_nowrap
	s_sub_u32 s3, s3, 11
.Lrot_nowrap:
	s_lshl_b32 s3, s3, 8
	s_add_u32 s8, s3, s94
